# speedup vs baseline: 1.0118x; 1.0118x over previous
_Z11proj_kernelPKfS0_S0_PKDF16_S0_S0_S0_PDF16_S3_S3_Pj:
	s_ashr_i32 s12, s2, 6
	s_load_dwordx8 s[4:11], s[0:1], 0x0
	s_cmp_gt_u32 s2, 63
	s_cselect_b64 s[22:23], -1, 0
	s_cmp_lg_u32 s12, 1
	s_cselect_b64 s[18:19], -1, 0
	s_cmp_eq_u32 s12, 1
	s_cselect_b64 s[20:21], -1, 0
	s_and_b64 s[14:15], s[20:21], exec
	s_waitcnt lgkmcnt(0)
	s_cselect_b32 s14, s6, s8
	s_cselect_b32 s15, s7, s9
	s_ashr_i32 s13, s12, 31
	s_lshl_b32 s28, s2, 7
	s_lshl_b64 s[6:7], s[12:13], 19
	s_and_b32 s3, s28, 0x1f80
	s_cmp_lt_u32 s2, 64
	s_cselect_b64 vcc, -1, 0
	v_lshrrev_b32_e32 v1, 2, v0
	v_or_b32_e32 v2, s3, v1
	s_and_b64 s[8:9], vcc, exec
	s_cselect_b32 s25, s5, s15
	s_cselect_b32 s24, s4, s14
	v_lshlrev_b32_e32 v2, 11, v2
	v_mov_b32_e32 v3, 0
	v_lshlrev_b32_e32 v6, 5, v0
	s_add_u32 s4, s10, s6
	v_lshl_add_u64 v[4:5], s[24:25], 0, v[2:3]
	v_and_b32_e32 v6, 0x60, v6
	v_mov_b32_e32 v7, v3
	v_lshlrev_b32_e32 v56, 4, v0
	v_mov_b32_e32 v57, v3
	s_addc_u32 s5, s11, s7
	v_lshl_add_u64 v[4:5], v[4:5], 0, v[6:7]
	s_movk_i32 s8, 0x2000
	v_lshl_add_u64 v[6:7], s[4:5], 0, v[56:57]
	global_load_dwordx4 v[8:11], v[4:5], off nt
	global_load_dwordx4 v[12:15], v[4:5], off offset:16 nt
	global_load_dwordx4 v[16:19], v56, s[4:5] sc1
	v_add_co_u32_e64 v28, s[4:5], s8, v6
	s_mov_b32 s33, 0xa000
	s_nop 0
	v_addc_co_u32_e64 v29, s[4:5], 0, v7, s[4:5]
	s_movk_i32 s4, 0x4000
	s_nop 0
	v_add_co_u32_e64 v30, s[4:5], s4, v6
	s_mov_b32 s6, 0xe000
	s_nop 0
	v_addc_co_u32_e64 v31, s[4:5], 0, v7, s[4:5]
	global_load_dwordx4 v[20:23], v[28:29], off sc1
	global_load_dwordx4 v[24:27], v[30:31], off sc1
	s_movk_i32 s4, 0x6000
	v_add_co_u32_e64 v40, s[4:5], s4, v6
	v_lshlrev_b32_e32 v57, 6, v1
	s_nop 0
	v_addc_co_u32_e64 v41, s[4:5], 0, v7, s[4:5]
	global_load_dwordx4 v[28:31], v[40:41], off sc1
	global_load_dwordx4 v[32:35], v[4:5], off offset:128 nt
	global_load_dwordx4 v[36:39], v[4:5], off offset:144 nt
	s_mov_b32 s4, 0x8000
	v_add_co_u32_e64 v40, s[4:5], s4, v6
	v_bitop3_b32 v58, v56, 48, v0 bitop3:0x48
	s_nop 0
	v_addc_co_u32_e64 v41, s[4:5], 0, v7, s[4:5]
	v_add_co_u32_e64 v44, s[4:5], s33, v6
	global_load_dwordx4 v[40:43], v[40:41], off sc1
	s_nop 0
	v_addc_co_u32_e64 v45, s[4:5], 0, v7, s[4:5]
	s_mov_b32 s4, 0xc000
	s_nop 0
	v_add_co_u32_e64 v48, s[4:5], s4, v6
	global_load_dwordx4 v[44:47], v[44:45], off sc1
	s_nop 0
	v_addc_co_u32_e64 v49, s[4:5], 0, v7, s[4:5]
	v_add_co_u32_e64 v52, s[4:5], s6, v6
	global_load_dwordx4 v[48:51], v[48:49], off sc1
	s_nop 0
	v_addc_co_u32_e64 v53, s[4:5], 0, v7, s[4:5]
	global_load_dwordx4 v[52:55], v[52:53], off sc1
	s_mov_b32 s4, 0x1e000
	v_add3_u32 v209, 0, v57, v58
	v_add_u32_e32 v208, 0, v56
	v_readfirstlane_b32 s30, v0
	v_bfe_u32 v207, v0, 5, 1
	v_bitop3_b32 v1, v207, v1, 3 bitop3:0x78
	v_lshlrev_b32_e32 v210, 4, v1
	s_mov_b32 s34, 0x14000
	v_add_u32_e32 v213, 0x2000, v208
	s_mov_b32 s43, 0
	s_lshr_b32 s29, s30, 6
	s_mov_b32 s35, -2
	s_mov_b32 s36, 0xffff2000
	s_mov_b32 s37, 0xffff4000
	s_mov_b32 s38, 0xffff6000
	s_movk_i32 s39, 0x8000
	s_movk_i32 s40, 0xa000
	s_movk_i32 s41, 0xc000
	s_movk_i32 s42, 0xe000
	s_mov_b64 s[26:27], 0x100
	v_mov_b32_e32 v56, v3
	v_mov_b32_e32 v57, v3
	v_mov_b32_e32 v58, v3
	v_mov_b32_e32 v59, v3
	v_mov_b32_e32 v60, v3
	v_mov_b32_e32 v61, v3
	v_mov_b32_e32 v62, v3
	v_mov_b32_e32 v63, v3
	v_mov_b32_e32 v64, v3
	v_mov_b32_e32 v65, v3
	v_mov_b32_e32 v66, v3
	v_mov_b32_e32 v67, v3
	v_mov_b32_e32 v68, v3
	v_mov_b32_e32 v69, v3
	v_mov_b32_e32 v70, v3
	s_waitcnt vmcnt(11)
	v_cvt_pk_f16_f32 v8, v8, v9
	v_cvt_pk_f16_f32 v9, v10, v11
	s_waitcnt vmcnt(10)
	v_cvt_pk_f16_f32 v10, v12, v13
	v_cvt_pk_f16_f32 v11, v14, v15
	ds_write_b128 v209, v[8:11]
	v_and_b32_e32 v10, 31, v0
	s_waitcnt vmcnt(9)
	ds_write_b128 v208, v[16:19] offset:8192
	s_waitcnt vmcnt(8)
	ds_write_b128 v208, v[20:23] offset:16384
	s_waitcnt vmcnt(7)
	ds_write_b128 v208, v[24:27] offset:24576
	s_load_dwordx2 s[16:17], s[0:1], 0x50
	s_load_dwordx4 s[12:15], s[0:1], 0x40
	s_load_dwordx8 s[4:11], s[0:1], 0x20
	s_lshl_b32 s0, s30, 1
	s_and_b32 s31, s0, 0x180
	s_lshr_b32 s0, s30, 2
	v_bfe_u32 v11, v0, 2, 2
	s_and_b32 s0, s0, 0x3fffffc0
	s_waitcnt vmcnt(5)
	v_cvt_pk_f16_f32 v8, v32, v33
	v_cvt_pk_f16_f32 v9, v34, v35
	v_or_b32_e32 v12, s31, v10
	v_or_b32_e32 v206, s0, v10
	v_bitop3_b32 v1, v207, v11, 2 bitop3:0x36
	s_waitcnt vmcnt(4)
	v_cvt_pk_f16_f32 v10, v36, v37
	v_cvt_pk_f16_f32 v11, v38, v39
	s_mov_b32 s0, 0x10000
	ds_write_b128 v208, v[28:31] offset:32768
	ds_write_b128 v209, v[8:11] offset:40960
	v_add_co_u32_e64 v8, s[0:1], s0, v6
	global_load_dwordx4 v[154:157], v[4:5], off offset:272 nt
	global_load_dwordx4 v[162:165], v[4:5], off offset:256 nt
	v_addc_co_u32_e64 v9, s[0:1], 0, v7, s[0:1]
	s_mov_b32 s0, 0x12000
	global_load_dwordx4 v[158:161], v[8:9], off sc1
	v_add_co_u32_e64 v8, s[0:1], s0, v6
	v_lshl_add_u32 v211, v12, 6, 0
	s_nop 0
	v_addc_co_u32_e64 v9, s[0:1], 0, v7, s[0:1]
	v_add_co_u32_e64 v10, s[0:1], s34, v6
	v_add_u32_e32 v14, 0x12000, v208
	s_nop 0
	v_addc_co_u32_e64 v11, s[0:1], 0, v7, s[0:1]
	s_mov_b32 s0, 0x16000
	s_nop 0
	v_add_co_u32_e64 v12, s[0:1], s0, v6
	s_waitcnt vmcnt(3)
	ds_write_b128 v14, v[52:55]
	v_addc_co_u32_e64 v13, s[0:1], 0, v7, s[0:1]
	s_mov_b32 s0, 0x18000
	s_nop 0
	v_add_co_u32_e64 v14, s[0:1], s0, v6
	ds_write_b128 v208, v[40:43] offset:49152
	s_nop 0
	v_addc_co_u32_e64 v15, s[0:1], 0, v7, s[0:1]
	s_mov_b32 s0, 0x1a000
	s_nop 0
	v_add_co_u32_e64 v16, s[0:1], s0, v6
	ds_write_b128 v208, v[44:47] offset:57344
	s_nop 0
	v_addc_co_u32_e64 v17, s[0:1], 0, v7, s[0:1]
	s_mov_b32 s0, 0x1c000
	ds_write_b128 v213, v[48:51] offset:57344
	v_add_co_u32_e64 v18, s[0:1], s0, v6
	v_add_u32_e32 v216, v211, v210
	s_nop 0
	v_addc_co_u32_e64 v19, s[0:1], 0, v7, s[0:1]
	global_load_dwordx4 v[174:177], v[8:9], off sc1
	global_load_dwordx4 v[166:169], v[10:11], off sc1
	global_load_dwordx4 v[170:173], v[12:13], off sc1
	global_load_dwordx4 v[142:145], v[4:5], off offset:400 nt
	global_load_dwordx4 v[150:153], v[4:5], off offset:384 nt
	global_load_dwordx4 v[138:141], v[14:15], off sc1
	global_load_dwordx4 v[146:149], v[16:17], off sc1
	global_load_dwordx4 v[134:137], v[18:19], off sc1
	s_mov_b32 s0, 0x1e000
	v_add_co_u32_e64 v8, s[0:1], s0, v6
	s_nop 1
	v_addc_co_u32_e64 v9, s[0:1], 0, v7, s[0:1]
	global_load_dwordx4 v[130:133], v[8:9], off sc1
	s_waitcnt lgkmcnt(0)
	s_barrier
	v_lshl_add_u32 v218, v206, 6, 0
	v_add_u32_e32 v217, v218, v210
	ds_read_b128 v[198:201], v216 offset:8192
	ds_read_b128 v[194:197], v216 offset:10240
	ds_read_b128 v[190:193], v216 offset:12288
	ds_read_b128 v[178:181], v216 offset:14336
	ds_read_b128 v[186:189], v217
	ds_read_b128 v[182:185], v217 offset:2048
	v_and_b32_e32 v20, 3, v0
	v_lshl_or_b32 v2, v20, 5, v2
	s_mov_b64 s[0:1], 0x2e000
	v_lshlrev_b32_e32 v212, 4, v1
	v_lshl_add_u64 v[202:203], v[6:7], 0, s[0:1]
	s_mov_b64 s[0:1], 0x290
	v_lshl_add_u64 v[4:5], s[24:25], 0, v[2:3]
	v_lshl_add_u64 v[204:205], v[4:5], 0, s[0:1]
	s_mov_b64 s[24:25], 0x10000
	v_mov_b32_e32 v2, v3
	v_mov_b32_e32 v4, v3
	v_mov_b32_e32 v5, v3
	v_mov_b32_e32 v6, v3
	v_mov_b32_e32 v7, v3
	v_mov_b32_e32 v8, v3
	v_mov_b32_e32 v9, v3
	v_mov_b32_e32 v10, v3
	v_mov_b32_e32 v11, v3
	v_mov_b32_e32 v12, v3
	v_mov_b32_e32 v13, v3
	v_mov_b32_e32 v14, v3
	v_mov_b32_e32 v15, v3
	v_mov_b32_e32 v16, v3
	v_mov_b32_e32 v17, v3
	v_mov_b32_e32 v18, v3
	v_mov_b32_e32 v19, v3
	v_mov_b32_e32 v20, v3
	v_mov_b32_e32 v21, v3
	v_mov_b32_e32 v22, v3
	v_mov_b32_e32 v23, v3
	v_mov_b32_e32 v24, v3
	v_mov_b32_e32 v25, v3
	v_mov_b32_e32 v26, v3
	v_mov_b32_e32 v27, v3
	v_mov_b32_e32 v28, v3
	v_mov_b32_e32 v29, v3
	v_mov_b32_e32 v30, v3
	v_mov_b32_e32 v31, v3
	v_mov_b32_e32 v32, v3
	v_mov_b32_e32 v33, v3
	v_mov_b32_e32 v34, v3
	v_mov_b32_e32 v35, v3
	v_mov_b32_e32 v36, v3
	v_mov_b32_e32 v37, v3
	v_mov_b32_e32 v38, v3
	v_mov_b32_e32 v39, v3
	v_mov_b32_e32 v40, v3
	v_mov_b32_e32 v41, v3
	v_mov_b32_e32 v42, v3
	v_mov_b32_e32 v43, v3
	v_mov_b32_e32 v44, v3
	v_mov_b32_e32 v45, v3
	v_mov_b32_e32 v46, v3
	v_mov_b32_e32 v47, v3
	v_mov_b32_e32 v48, v3
	v_mov_b32_e32 v49, v3
	v_mov_b32_e32 v50, v3
	v_mov_b32_e32 v51, v3
	v_mov_b32_e32 v52, v3
	v_mov_b32_e32 v53, v3
	v_mov_b32_e32 v54, v3
	v_mov_b32_e32 v55, v3
	v_mov_b32_e32 v71, v3
	v_mov_b32_e32 v72, v3
	v_mov_b32_e32 v73, v3
	v_mov_b32_e32 v74, v3
	v_mov_b32_e32 v75, v3
	v_mov_b32_e32 v76, v3
	v_mov_b32_e32 v77, v3
	v_mov_b32_e32 v78, v3
	v_mov_b32_e32 v79, v3
	v_mov_b32_e32 v80, v3
	v_mov_b32_e32 v81, v3
	v_mov_b32_e32 v82, v3
	v_mov_b32_e32 v83, v3
	v_mov_b32_e32 v84, v3
	v_mov_b32_e32 v85, v3
	v_mov_b32_e32 v86, v3
	v_mov_b32_e32 v87, v3
	v_mov_b32_e32 v88, v3
	v_mov_b32_e32 v89, v3
	v_mov_b32_e32 v90, v3
	v_mov_b32_e32 v91, v3
	v_mov_b32_e32 v92, v3
	v_mov_b32_e32 v93, v3
	v_mov_b32_e32 v94, v3
	v_mov_b32_e32 v95, v3
	v_mov_b32_e32 v96, v3
	v_mov_b32_e32 v97, v3
	v_mov_b32_e32 v98, v3
	v_mov_b32_e32 v99, v3
	v_mov_b32_e32 v100, v3
	v_mov_b32_e32 v101, v3
	v_mov_b32_e32 v102, v3
	v_mov_b32_e32 v103, v3
	v_mov_b32_e32 v104, v3
	v_mov_b32_e32 v105, v3
	v_mov_b32_e32 v106, v3
	v_mov_b32_e32 v107, v3
	v_mov_b32_e32 v108, v3
	v_mov_b32_e32 v109, v3
	v_mov_b32_e32 v110, v3
	v_mov_b32_e32 v111, v3
	v_mov_b32_e32 v112, v3
	v_mov_b32_e32 v113, v3
	v_mov_b32_e32 v114, v3
	v_mov_b32_e32 v115, v3
	v_mov_b32_e32 v116, v3
	v_mov_b32_e32 v117, v3
	v_mov_b32_e32 v118, v3
	v_mov_b32_e32 v119, v3
	v_mov_b32_e32 v120, v3
	v_mov_b32_e32 v121, v3
	v_mov_b32_e32 v122, v3
	v_mov_b32_e32 v123, v3
	v_mov_b32_e32 v124, v3
	v_mov_b32_e32 v125, v3
	v_mov_b32_e32 v126, v3
	v_mov_b32_e32 v127, v3
	v_mov_b32_e32 v128, v3
	v_mov_b32_e32 v129, v3
	v_and_b32_e32 v1, 63, v0
	v_add_u32_e32 v215, v211, v212
	v_add_u32_e32 v214, v218, v212
.LBB1_1:
	s_waitcnt lgkmcnt(0)
	v_mfma_f32_32x32x16_f16 v[114:129], v[198:201], v[186:189], v[114:129]
	s_mov_b32 s44, s33
	s_mov_b32 s33, s43
	v_mfma_f32_32x32x16_f16 v[98:113], v[198:201], v[182:185], v[98:113]
	v_add_u32_e32 v219, s33, v215
	ds_read_b128 v[198:201], v219 offset:8192
	ds_read_b128 v[220:223], v219 offset:10240
	ds_read_b128 v[224:227], v219 offset:12288
	ds_read_b128 v[228:231], v219 offset:14336
	v_add_u32_e32 v219, s33, v214
	ds_read_b128 v[232:235], v219
	ds_read_b128 v[236:239], v219 offset:2048
	s_waitcnt vmcnt(10)
	v_cvt_pk_f16_f32 v162, v162, v163
	v_cvt_pk_f16_f32 v163, v164, v165
	v_cvt_pk_f16_f32 v164, v154, v155
	v_cvt_pk_f16_f32 v165, v156, v157
	v_add_u32_e32 v154, s34, v209
	ds_write_b128 v154, v[162:165]
	v_mfma_f32_32x32x16_f16 v[82:97], v[194:197], v[186:189], v[82:97]
	v_add_u32_e32 v154, s34, v208
	s_waitcnt vmcnt(9)
	ds_write_b128 v154, v[158:161] offset:8192
	s_waitcnt vmcnt(8)
	ds_write_b128 v154, v[174:177] offset:16384
	v_mfma_f32_32x32x16_f16 v[66:81], v[194:197], v[182:185], v[66:81]
	v_mfma_f32_32x32x16_f16 v[50:65], v[190:193], v[186:189], v[50:65]
	s_waitcnt vmcnt(7)
	ds_write_b128 v154, v[166:169] offset:24576
	s_waitcnt vmcnt(6)
	ds_write_b128 v154, v[170:173] offset:32768
	v_mfma_f32_32x32x16_f16 v[34:49], v[190:193], v[182:185], v[34:49]
	v_add_co_u32_e64 v158, s[0:1], s36, v202
	global_load_dwordx4 v[154:157], v[204:205], off offset:-128 nt
	global_load_dwordx4 v[162:165], v[204:205], off offset:-144 nt
	v_addc_co_u32_e64 v159, s[0:1], -1, v203, s[0:1]
	v_add_co_u32_e64 v166, s[0:1], s37, v202
	v_mfma_f32_32x32x16_f16 v[18:33], v[178:181], v[186:189], v[18:33]
	s_nop 0
	v_addc_co_u32_e64 v167, s[0:1], -1, v203, s[0:1]
	global_load_dwordx4 v[158:161], v[158:159], off sc1
	s_nop 0
	global_load_dwordx4 v[174:177], v[166:167], off sc1
	v_add_co_u32_e64 v166, s[0:1], s38, v202
	s_nop 1
	v_addc_co_u32_e64 v167, s[0:1], -1, v203, s[0:1]
	v_add_co_u32_e64 v170, s[0:1], s39, v202
	v_mfma_f32_32x32x16_f16 v[2:17], v[178:181], v[182:185], v[2:17]
	s_nop 0
	v_addc_co_u32_e64 v171, s[0:1], -1, v203, s[0:1]
	global_load_dwordx4 v[166:169], v[166:167], off sc1
	s_nop 0
	global_load_dwordx4 v[170:173], v[170:171], off sc1
	v_add_u32_e32 v190, s44, v216
	ds_read_b128 v[178:181], v190 offset:8192
	ds_read_b128 v[182:185], v190 offset:10240
	ds_read_b128 v[186:189], v190 offset:12288
	ds_read_b128 v[190:193], v190 offset:14336
	v_add_u32_e32 v219, s44, v217
	ds_read_b128 v[194:197], v219
	ds_read_b128 v[240:243], v219 offset:2048
	s_waitcnt lgkmcnt(12)
	v_mfma_f32_32x32x16_f16 v[114:129], v[198:201], v[232:235], v[114:129]
	s_waitcnt lgkmcnt(11)
	v_mfma_f32_32x32x16_f16 v[98:113], v[198:201], v[236:239], v[98:113]
	v_mfma_f32_32x32x16_f16 v[82:97], v[220:223], v[232:235], v[82:97]
	v_mfma_f32_32x32x16_f16 v[66:81], v[220:223], v[236:239], v[66:81]
	v_mfma_f32_32x32x16_f16 v[50:65], v[224:227], v[232:235], v[50:65]
	v_mfma_f32_32x32x16_f16 v[34:49], v[224:227], v[236:239], v[34:49]
	v_mfma_f32_32x32x16_f16 v[18:33], v[228:231], v[232:235], v[18:33]
	v_mfma_f32_32x32x16_f16 v[2:17], v[228:231], v[236:239], v[2:17]
	s_waitcnt lgkmcnt(1)
	v_mfma_f32_32x32x16_f16 v[114:129], v[178:181], v[194:197], v[114:129]
	s_waitcnt lgkmcnt(0)
	s_barrier
	s_waitcnt lgkmcnt(0)
	v_mfma_f32_32x32x16_f16 v[98:113], v[178:181], v[240:243], v[98:113]
	v_add_u32_e32 v178, s44, v215
	ds_read_b128 v[220:223], v178 offset:8192
	ds_read_b128 v[224:227], v178 offset:10240
	ds_read_b128 v[228:231], v178 offset:12288
	ds_read_b128 v[232:235], v178 offset:14336
	v_add_u32_e32 v178, s44, v214
	ds_read_b128 v[236:239], v178
	ds_read_b128 v[244:247], v178 offset:2048
	s_waitcnt vmcnt(10)
	v_cvt_pk_f16_f32 v150, v150, v151
	v_cvt_pk_f16_f32 v151, v152, v153
	v_cvt_pk_f16_f32 v152, v142, v143
	v_cvt_pk_f16_f32 v153, v144, v145
	v_add_u32_e32 v142, s33, v209
	ds_write_b128 v142, v[150:153]
	v_mfma_f32_32x32x16_f16 v[82:97], v[182:185], v[194:197], v[82:97]
	v_add_u32_e32 v142, s33, v208
	s_waitcnt vmcnt(9)
	ds_write_b128 v142, v[138:141] offset:8192
	s_waitcnt vmcnt(8)
	ds_write_b128 v142, v[146:149] offset:16384
	v_mfma_f32_32x32x16_f16 v[66:81], v[182:185], v[240:243], v[66:81]
	v_mfma_f32_32x32x16_f16 v[50:65], v[186:189], v[194:197], v[50:65]
	s_waitcnt vmcnt(7)
	ds_write_b128 v142, v[134:137] offset:24576
	s_waitcnt vmcnt(6)
	ds_write_b128 v142, v[130:133] offset:32768
	v_mfma_f32_32x32x16_f16 v[34:49], v[186:189], v[240:243], v[34:49]
	v_add_co_u32_e64 v130, s[0:1], s40, v202
	global_load_dwordx4 v[142:145], v[204:205], off nt
	global_load_dwordx4 v[150:153], v[204:205], off offset:-16 nt
	v_addc_co_u32_e64 v131, s[0:1], -1, v203, s[0:1]
	v_add_co_u32_e64 v132, s[0:1], s41, v202
	v_mfma_f32_32x32x16_f16 v[18:33], v[190:193], v[194:197], v[18:33]
	s_nop 0
	v_addc_co_u32_e64 v133, s[0:1], -1, v203, s[0:1]
	global_load_dwordx4 v[138:141], v[130:131], off sc1
	global_load_dwordx4 v[146:149], v[132:133], off sc1
	v_add_co_u32_e64 v130, s[0:1], s42, v202
	s_nop 1
	v_addc_co_u32_e64 v131, s[0:1], -1, v203, s[0:1]
	global_load_dwordx4 v[134:137], v[130:131], off sc1
	s_nop 0
	global_load_dwordx4 v[130:133], v[202:203], off sc1
	v_mfma_f32_32x32x16_f16 v[2:17], v[190:193], v[240:243], v[2:17]
	v_add_u32_e32 v178, s34, v216
	ds_read_b128 v[198:201], v178 offset:8192
	ds_read_b128 v[194:197], v178 offset:10240
	ds_read_b128 v[190:193], v178 offset:12288
	ds_read_b128 v[178:181], v178 offset:14336
	v_add_u32_e32 v182, s34, v217
	ds_read_b128 v[186:189], v182
	ds_read_b128 v[182:185], v182 offset:2048
	s_waitcnt lgkmcnt(12)
	v_mfma_f32_32x32x16_f16 v[114:129], v[220:223], v[236:239], v[114:129]
	s_waitcnt lgkmcnt(11)
	v_mfma_f32_32x32x16_f16 v[98:113], v[220:223], v[244:247], v[98:113]
	v_mfma_f32_32x32x16_f16 v[82:97], v[224:227], v[236:239], v[82:97]
	v_mfma_f32_32x32x16_f16 v[66:81], v[224:227], v[244:247], v[66:81]
	v_mfma_f32_32x32x16_f16 v[50:65], v[228:231], v[236:239], v[50:65]
	v_mfma_f32_32x32x16_f16 v[34:49], v[228:231], v[244:247], v[34:49]
	v_mfma_f32_32x32x16_f16 v[18:33], v[232:235], v[236:239], v[18:33]
	v_mfma_f32_32x32x16_f16 v[2:17], v[232:235], v[244:247], v[2:17]
	s_waitcnt lgkmcnt(0)
	s_barrier
	s_add_i32 s35, s35, 2
	v_lshl_add_u64 v[202:203], v[202:203], 0, s[24:25]
	v_lshl_add_u64 v[204:205], v[204:205], 0, s[26:27]
	s_mov_b32 s43, s34
	s_cmp_gt_u32 s35, 9
	s_mov_b32 s34, s44
	s_cbranch_scc0 .LBB1_1
	s_and_b64 s[0:1], s[20:21], exec
	s_cselect_b32 s6, s6, s8
	s_cselect_b32 s7, s7, s9
	s_and_b64 s[0:1], vcc, exec
	s_cselect_b32 s1, s5, s7
	s_cselect_b32 s0, s4, s6
	v_mov_b32_e32 v202, 0x3e38aa3b
	s_waitcnt lgkmcnt(1)
	v_mfma_f32_32x32x16_f16 v[114:129], v[198:201], v[186:189], v[114:129]
	v_cndmask_b32_e32 v202, 1.0, v202, vcc
	s_waitcnt lgkmcnt(0)
	v_mfma_f32_32x32x16_f16 v[98:113], v[198:201], v[182:185], v[98:113]
	ds_read_b128 v[198:201], v215 offset:8192
	ds_read_b128 v[220:223], v215 offset:10240
	ds_read_b128 v[224:227], v215 offset:12288
	ds_read_b128 v[228:231], v215 offset:14336
	ds_read_b128 v[232:235], v214
	ds_read_b128 v[236:239], v214 offset:2048
	s_waitcnt vmcnt(10)
	v_cvt_pk_f16_f32 v162, v162, v163
	v_cvt_pk_f16_f32 v163, v164, v165
	v_cvt_pk_f16_f32 v164, v154, v155
	v_cvt_pk_f16_f32 v165, v156, v157
	v_add_u32_e32 v154, 0x14000, v209
	ds_write_b128 v154, v[162:165]
	v_add_u32_e32 v154, 0x14000, v213
	s_waitcnt vmcnt(9)
	ds_write_b128 v154, v[158:161]
	v_add_u32_e32 v154, 0x16000, v213
	v_mfma_f32_32x32x16_f16 v[82:97], v[194:197], v[186:189], v[82:97]
	s_waitcnt vmcnt(8)
	ds_write_b128 v154, v[174:177]
	v_mfma_f32_32x32x16_f16 v[66:81], v[194:197], v[182:185], v[66:81]
	v_add_u32_e32 v154, 0x18000, v213
	s_waitcnt vmcnt(7)
	ds_write_b128 v154, v[166:169]
	v_add_u32_e32 v154, 0x1a000, v213
	v_mfma_f32_32x32x16_f16 v[50:65], v[190:193], v[186:189], v[50:65]
	s_waitcnt vmcnt(6)
	ds_write_b128 v154, v[170:173]
	v_mfma_f32_32x32x16_f16 v[34:49], v[190:193], v[182:185], v[34:49]
	v_mfma_f32_32x32x16_f16 v[18:33], v[178:181], v[186:189], v[18:33]
	v_mfma_f32_32x32x16_f16 v[2:17], v[178:181], v[182:185], v[2:17]
	ds_read_b128 v[154:157], v216 offset:49152
	ds_read_b128 v[158:161], v216 offset:51200
	ds_read_b128 v[162:165], v216 offset:53248
	ds_read_b128 v[166:169], v216 offset:55296
	ds_read_b128 v[170:173], v217 offset:40960
	ds_read_b128 v[174:177], v217 offset:43008
	s_waitcnt lgkmcnt(12)
	v_mfma_f32_32x32x16_f16 v[114:129], v[198:201], v[232:235], v[114:129]
	s_waitcnt lgkmcnt(11)
	v_mfma_f32_32x32x16_f16 v[98:113], v[198:201], v[236:239], v[98:113]
	v_mfma_f32_32x32x16_f16 v[82:97], v[220:223], v[232:235], v[82:97]
	v_mfma_f32_32x32x16_f16 v[66:81], v[220:223], v[236:239], v[66:81]
	v_mfma_f32_32x32x16_f16 v[50:65], v[224:227], v[232:235], v[50:65]
	v_mfma_f32_32x32x16_f16 v[34:49], v[224:227], v[236:239], v[34:49]
	v_mfma_f32_32x32x16_f16 v[18:33], v[228:231], v[232:235], v[18:33]
	v_mfma_f32_32x32x16_f16 v[2:17], v[228:231], v[236:239], v[2:17]
	s_waitcnt lgkmcnt(0)
	s_barrier
	s_waitcnt lgkmcnt(1)
	v_mfma_f32_32x32x16_f16 v[114:129], v[154:157], v[170:173], v[114:129]
	s_waitcnt lgkmcnt(0)
	v_mfma_f32_32x32x16_f16 v[98:113], v[154:157], v[174:177], v[98:113]
	ds_read_b128 v[154:157], v215 offset:49152
	ds_read_b128 v[178:181], v215 offset:51200
	ds_read_b128 v[182:185], v215 offset:53248
	ds_read_b128 v[186:189], v215 offset:55296
	ds_read_b128 v[190:193], v214 offset:40960
	ds_read_b128 v[194:197], v214 offset:43008
	s_waitcnt vmcnt(4)
	v_cvt_pk_f16_f32 v150, v150, v151
	v_cvt_pk_f16_f32 v151, v152, v153
	v_cvt_pk_f16_f32 v152, v142, v143
	v_cvt_pk_f16_f32 v153, v144, v145
	ds_write_b128 v209, v[150:153]
	v_mfma_f32_32x32x16_f16 v[82:97], v[158:161], v[170:173], v[82:97]
	s_waitcnt vmcnt(3)
	ds_write_b128 v208, v[138:141] offset:8192
	s_waitcnt vmcnt(2)
	ds_write_b128 v208, v[146:149] offset:16384
	v_mfma_f32_32x32x16_f16 v[66:81], v[158:161], v[174:177], v[66:81]
	v_mfma_f32_32x32x16_f16 v[50:65], v[162:165], v[170:173], v[50:65]
	s_waitcnt vmcnt(1)
	ds_write_b128 v208, v[134:137] offset:24576
	s_waitcnt vmcnt(0)
	ds_write_b128 v208, v[130:133] offset:32768
	v_mfma_f32_32x32x16_f16 v[34:49], v[162:165], v[174:177], v[34:49]
	v_mfma_f32_32x32x16_f16 v[18:33], v[166:169], v[170:173], v[18:33]
	v_mfma_f32_32x32x16_f16 v[2:17], v[166:169], v[174:177], v[2:17]
	v_add_u32_e32 v158, 0x16000, v211
	v_add_u32_e32 v142, v158, v210
	ds_read_b128 v[130:133], v142
	ds_read_b128 v[134:137], v142 offset:2048
	ds_read_b128 v[138:141], v142 offset:4096
	ds_read_b128 v[142:145], v142 offset:6144
	v_add_u32_e32 v166, 0x14000, v218
	v_add_u32_e32 v150, v166, v210
	ds_read_b128 v[146:149], v150
	ds_read_b128 v[150:153], v150 offset:2048
	s_waitcnt lgkmcnt(12)
	v_mfma_f32_32x32x16_f16 v[114:129], v[154:157], v[190:193], v[114:129]
	s_waitcnt lgkmcnt(11)
	v_mfma_f32_32x32x16_f16 v[98:113], v[154:157], v[194:197], v[98:113]
	v_mfma_f32_32x32x16_f16 v[82:97], v[178:181], v[190:193], v[82:97]
	v_mfma_f32_32x32x16_f16 v[66:81], v[178:181], v[194:197], v[66:81]
	v_mfma_f32_32x32x16_f16 v[50:65], v[182:185], v[190:193], v[50:65]
	v_mfma_f32_32x32x16_f16 v[34:49], v[182:185], v[194:197], v[34:49]
	v_mfma_f32_32x32x16_f16 v[18:33], v[186:189], v[190:193], v[18:33]
	v_mfma_f32_32x32x16_f16 v[2:17], v[186:189], v[194:197], v[2:17]
	s_waitcnt lgkmcnt(0)
	s_barrier
	s_waitcnt lgkmcnt(1)
	v_mfma_f32_32x32x16_f16 v[114:129], v[130:133], v[146:149], v[114:129]
	s_waitcnt lgkmcnt(0)
	v_mfma_f32_32x32x16_f16 v[98:113], v[130:133], v[150:153], v[98:113]
	v_add_u32_e32 v162, v158, v212
	ds_read_b128 v[130:133], v162
	ds_read_b128 v[154:157], v162 offset:2048
	ds_read_b128 v[158:161], v162 offset:4096
	ds_read_b128 v[162:165], v162 offset:6144
	v_add_u32_e32 v170, v166, v212
	ds_read_b128 v[166:169], v170
	ds_read_b128 v[170:173], v170 offset:2048
	v_mfma_f32_32x32x16_f16 v[82:97], v[134:137], v[146:149], v[82:97]
	v_mfma_f32_32x32x16_f16 v[66:81], v[134:137], v[150:153], v[66:81]
	v_mfma_f32_32x32x16_f16 v[50:65], v[138:141], v[146:149], v[50:65]
	v_mfma_f32_32x32x16_f16 v[34:49], v[138:141], v[150:153], v[34:49]
	v_mfma_f32_32x32x16_f16 v[18:33], v[142:145], v[146:149], v[18:33]
	v_mfma_f32_32x32x16_f16 v[2:17], v[142:145], v[150:153], v[2:17]
	ds_read_b128 v[134:137], v216 offset:8192
	ds_read_b128 v[138:141], v216 offset:10240
	ds_read_b128 v[142:145], v216 offset:12288
	ds_read_b128 v[146:149], v216 offset:14336
	ds_read_b128 v[150:153], v217
	ds_read_b128 v[174:177], v217 offset:2048
	s_waitcnt lgkmcnt(7)
	v_mfma_f32_32x32x16_f16 v[114:129], v[130:133], v[166:169], v[114:129]
	s_waitcnt lgkmcnt(6)
	v_mfma_f32_32x32x16_f16 v[98:113], v[130:133], v[170:173], v[98:113]
	v_mfma_f32_32x32x16_f16 v[82:97], v[154:157], v[166:169], v[82:97]
	v_mfma_f32_32x32x16_f16 v[66:81], v[154:157], v[170:173], v[66:81]
	v_mfma_f32_32x32x16_f16 v[50:65], v[158:161], v[166:169], v[50:65]
	v_mfma_f32_32x32x16_f16 v[34:49], v[158:161], v[170:173], v[34:49]
	v_mfma_f32_32x32x16_f16 v[18:33], v[162:165], v[166:169], v[18:33]
	v_mfma_f32_32x32x16_f16 v[2:17], v[162:165], v[170:173], v[2:17]
	s_waitcnt lgkmcnt(0)
	s_barrier
	s_waitcnt lgkmcnt(1)
	v_mfma_f32_32x32x16_f16 v[114:129], v[134:137], v[150:153], v[114:129]
	s_waitcnt lgkmcnt(0)
	v_mfma_f32_32x32x16_f16 v[98:113], v[134:137], v[174:177], v[98:113]
	ds_read_b128 v[130:133], v215 offset:8192
	ds_read_b128 v[134:137], v215 offset:10240
	ds_read_b128 v[154:157], v215 offset:12288
	ds_read_b128 v[158:161], v215 offset:14336
	ds_read_b128 v[162:165], v214
	ds_read_b128 v[166:169], v214 offset:2048
	v_mfma_f32_32x32x16_f16 v[82:97], v[138:141], v[150:153], v[82:97]
	v_mfma_f32_32x32x16_f16 v[66:81], v[138:141], v[174:177], v[66:81]
	v_mfma_f32_32x32x16_f16 v[50:65], v[142:145], v[150:153], v[50:65]
	v_mfma_f32_32x32x16_f16 v[34:49], v[142:145], v[174:177], v[34:49]
	v_mfma_f32_32x32x16_f16 v[18:33], v[146:149], v[150:153], v[18:33]
	v_mfma_f32_32x32x16_f16 v[2:17], v[146:149], v[174:177], v[2:17]
	s_waitcnt lgkmcnt(1)
	v_mfma_f32_32x32x16_f16 v[114:129], v[130:133], v[162:165], v[114:129]
	s_waitcnt lgkmcnt(0)
	v_mfma_f32_32x32x16_f16 v[98:113], v[130:133], v[166:169], v[98:113]
	v_mfma_f32_32x32x16_f16 v[82:97], v[134:137], v[162:165], v[82:97]
	v_mfma_f32_32x32x16_f16 v[66:81], v[134:137], v[166:169], v[66:81]
	v_mfma_f32_32x32x16_f16 v[50:65], v[154:157], v[162:165], v[50:65]
	v_mfma_f32_32x32x16_f16 v[34:49], v[154:157], v[166:169], v[34:49]
	v_mfma_f32_32x32x16_f16 v[18:33], v[158:161], v[162:165], v[18:33]
	v_mfma_f32_32x32x16_f16 v[2:17], v[158:161], v[166:169], v[2:17]
	v_lshl_or_b32 v130, v207, 2, s31
	s_waitcnt lgkmcnt(0)
	s_barrier
	v_lshlrev_b32_e32 v154, 2, v130
	global_load_dwordx4 v[134:137], v154, s[0:1]
	global_load_dwordx4 v[150:153], v154, s[0:1] offset:32
	global_load_dwordx4 v[156:159], v154, s[0:1] offset:64
	global_load_dwordx4 v[160:163], v154, s[0:1] offset:96
	global_load_dwordx4 v[164:167], v154, s[0:1] offset:128
	global_load_dwordx4 v[168:171], v154, s[0:1] offset:160
	s_movk_i32 s4, 0x410
	v_lshlrev_b32_e32 v130, 1, v130
	v_mul_lo_u32 v131, v206, s4
	v_add3_u32 v155, 0, v130, v131
	global_load_dwordx4 v[172:175], v154, s[0:1] offset:192
	global_load_dwordx4 v[146:149], v154, s[0:1] offset:224
	global_load_dwordx4 v[142:145], v154, s[0:1] offset:256
	global_load_dwordx4 v[130:133], v154, s[0:1] offset:288
	global_load_dwordx4 v[138:141], v154, s[0:1] offset:320
	v_add_u32_e32 v176, 0x8000, v155
	s_waitcnt vmcnt(10)
	v_pk_add_f32 v[114:115], v[134:135], v[114:115]
	v_pk_add_f32 v[116:117], v[136:137], v[116:117]
	v_pk_add_f32 v[98:99], v[134:135], v[98:99]
	v_pk_add_f32 v[100:101], v[136:137], v[100:101]
	s_waitcnt vmcnt(9)
	v_pk_add_f32 v[118:119], v[150:151], v[118:119]
	v_pk_add_f32 v[120:121], v[152:153], v[120:121]
	s_waitcnt vmcnt(6)
	v_pk_add_f32 v[82:83], v[164:165], v[82:83]
	v_pk_add_f32 v[84:85], v[166:167], v[84:85]
	v_pk_add_f32 v[66:67], v[164:165], v[66:67]
	v_pk_add_f32 v[68:69], v[166:167], v[68:69]
	s_waitcnt vmcnt(5)
	v_pk_add_f32 v[70:71], v[168:169], v[70:71]
	v_pk_add_f32 v[72:73], v[170:171], v[72:73]
	v_pk_add_f32 v[102:103], v[150:151], v[102:103]
	v_pk_add_f32 v[104:105], v[152:153], v[104:105]
	v_pk_add_f32 v[122:123], v[156:157], v[122:123]
	v_pk_add_f32 v[124:125], v[158:159], v[124:125]
	v_pk_add_f32 v[106:107], v[156:157], v[106:107]
	v_pk_add_f32 v[108:109], v[158:159], v[108:109]
	v_pk_add_f32 v[126:127], v[160:161], v[126:127]
	v_pk_add_f32 v[128:129], v[162:163], v[128:129]
	v_pk_add_f32 v[110:111], v[160:161], v[110:111]
	v_pk_add_f32 v[112:113], v[162:163], v[112:113]
	v_pk_add_f32 v[86:87], v[168:169], v[86:87]
	v_pk_mul_f32 v[114:115], v[202:203], v[114:115] op_sel_hi:[0,1]
	v_pk_mul_f32 v[116:117], v[202:203], v[116:117] op_sel_hi:[0,1]
	v_pk_mul_f32 v[98:99], v[202:203], v[98:99] op_sel_hi:[0,1]
	v_pk_mul_f32 v[100:101], v[202:203], v[100:101] op_sel_hi:[0,1]
	v_pk_mul_f32 v[118:119], v[202:203], v[118:119] op_sel_hi:[0,1]
	v_pk_mul_f32 v[120:121], v[202:203], v[120:121] op_sel_hi:[0,1]
	v_pk_mul_f32 v[82:83], v[202:203], v[82:83] op_sel_hi:[0,1]
	v_pk_mul_f32 v[84:85], v[202:203], v[84:85] op_sel_hi:[0,1]
	v_pk_mul_f32 v[66:67], v[202:203], v[66:67] op_sel_hi:[0,1]
	v_pk_mul_f32 v[68:69], v[202:203], v[68:69] op_sel_hi:[0,1]
	v_pk_add_f32 v[88:89], v[170:171], v[88:89]
	v_pk_mul_f32 v[70:71], v[202:203], v[70:71] op_sel_hi:[0,1]
	v_pk_mul_f32 v[72:73], v[202:203], v[72:73] op_sel_hi:[0,1]
	v_pk_mul_f32 v[102:103], v[202:203], v[102:103] op_sel_hi:[0,1]
	v_pk_mul_f32 v[104:105], v[202:203], v[104:105] op_sel_hi:[0,1]
	v_pk_mul_f32 v[122:123], v[202:203], v[122:123] op_sel_hi:[0,1]
	v_pk_mul_f32 v[124:125], v[202:203], v[124:125] op_sel_hi:[0,1]
	v_pk_mul_f32 v[106:107], v[202:203], v[106:107] op_sel_hi:[0,1]
	v_pk_mul_f32 v[108:109], v[202:203], v[108:109] op_sel_hi:[0,1]
	v_pk_mul_f32 v[126:127], v[202:203], v[126:127] op_sel_hi:[0,1]
	v_pk_mul_f32 v[128:129], v[202:203], v[128:129] op_sel_hi:[0,1]
	v_pk_mul_f32 v[110:111], v[202:203], v[110:111] op_sel_hi:[0,1]
	v_pk_mul_f32 v[112:113], v[202:203], v[112:113] op_sel_hi:[0,1]
	v_pk_mul_f32 v[86:87], v[202:203], v[86:87] op_sel_hi:[0,1]
	v_cvt_pk_f16_f32 v114, v114, v115
	v_cvt_pk_f16_f32 v115, v116, v117
	v_cvt_pk_f16_f32 v98, v98, v99
	v_cvt_pk_f16_f32 v99, v100, v101
	v_cvt_pk_f16_f32 v100, v118, v119
	v_cvt_pk_f16_f32 v101, v120, v121
	v_cvt_pk_f16_f32 v82, v82, v83
	v_cvt_pk_f16_f32 v83, v84, v85
	v_cvt_pk_f16_f32 v84, v66, v67
	v_cvt_pk_f16_f32 v85, v68, v69
	v_pk_mul_f32 v[88:89], v[202:203], v[88:89] op_sel_hi:[0,1]
	v_cvt_pk_f16_f32 v70, v70, v71
	v_cvt_pk_f16_f32 v71, v72, v73
	v_cvt_pk_f16_f32 v102, v102, v103
	v_cvt_pk_f16_f32 v103, v104, v105
	v_cvt_pk_f16_f32 v104, v122, v123
	v_cvt_pk_f16_f32 v105, v124, v125
	v_cvt_pk_f16_f32 v106, v106, v107
	v_cvt_pk_f16_f32 v107, v108, v109
	v_cvt_pk_f16_f32 v108, v126, v127
	v_cvt_pk_f16_f32 v109, v128, v129
	v_cvt_pk_f16_f32 v110, v110, v111
	v_cvt_pk_f16_f32 v111, v112, v113
	v_cvt_pk_f16_f32 v86, v86, v87
	ds_write2_b64 v155, v[114:115], v[100:101] offset1:2
	ds_write2_b64 v176, v[98:99], v[102:103] offset0:64 offset1:66
	ds_write2_b64 v155, v[104:105], v[108:109] offset0:4 offset1:6
	ds_write2_b64 v176, v[106:107], v[110:111] offset0:68 offset1:70
	v_cvt_pk_f16_f32 v87, v88, v89
	ds_write2_b64 v176, v[84:85], v[70:71] offset0:72 offset1:74
	s_waitcnt vmcnt(4)
	v_pk_add_f32 v[70:71], v[172:173], v[90:91]
	v_pk_add_f32 v[84:85], v[174:175], v[92:93]
	v_pk_add_f32 v[74:75], v[172:173], v[74:75]
	ds_write2_b64 v155, v[82:83], v[86:87] offset0:8 offset1:10
	v_pk_mul_f32 v[82:83], v[202:203], v[70:71] op_sel_hi:[0,1]
	v_pk_mul_f32 v[84:85], v[202:203], v[84:85] op_sel_hi:[0,1]
	v_pk_mul_f32 v[74:75], v[202:203], v[74:75] op_sel_hi:[0,1]
	global_load_dwordx4 v[66:69], v154, s[0:1] offset:352
	global_load_dwordx4 v[70:73], v154, s[0:1] offset:384
	v_cvt_pk_f16_f32 v82, v82, v83
	v_cvt_pk_f16_f32 v83, v84, v85
	v_cvt_pk_f16_f32 v84, v74, v75
	v_pk_add_f32 v[74:75], v[174:175], v[76:77]
	s_waitcnt vmcnt(5)
	v_pk_add_f32 v[78:79], v[146:147], v[78:79]
	v_pk_mul_f32 v[74:75], v[202:203], v[74:75] op_sel_hi:[0,1]
	v_cvt_pk_f16_f32 v85, v74, v75
	global_load_dwordx4 v[74:77], v154, s[0:1] offset:416
	v_pk_add_f32 v[80:81], v[148:149], v[80:81]
	v_pk_mul_f32 v[78:79], v[202:203], v[78:79] op_sel_hi:[0,1]
	v_pk_mul_f32 v[80:81], v[202:203], v[80:81] op_sel_hi:[0,1]
	v_cvt_pk_f16_f32 v78, v78, v79
	v_cvt_pk_f16_f32 v79, v80, v81
	ds_write2_b64 v176, v[84:85], v[78:79] offset0:76 offset1:78
	global_load_dwordx4 v[78:81], v154, s[0:1] offset:448
	v_pk_add_f32 v[86:87], v[146:147], v[94:95]
	v_pk_add_f32 v[88:89], v[148:149], v[96:97]
	s_waitcnt vmcnt(6)
	v_pk_add_f32 v[50:51], v[142:143], v[50:51]
	v_pk_add_f32 v[52:53], v[144:145], v[52:53]
	v_pk_add_f32 v[34:35], v[142:143], v[34:35]
	v_pk_mul_f32 v[86:87], v[202:203], v[86:87] op_sel_hi:[0,1]
	v_pk_mul_f32 v[88:89], v[202:203], v[88:89] op_sel_hi:[0,1]
	v_pk_mul_f32 v[50:51], v[202:203], v[50:51] op_sel_hi:[0,1]
	v_pk_mul_f32 v[52:53], v[202:203], v[52:53] op_sel_hi:[0,1]
	v_pk_mul_f32 v[34:35], v[202:203], v[34:35] op_sel_hi:[0,1]
	v_cvt_pk_f16_f32 v86, v86, v87
	v_cvt_pk_f16_f32 v87, v88, v89
	v_cvt_pk_f16_f32 v50, v50, v51
	v_cvt_pk_f16_f32 v51, v52, v53
	v_cvt_pk_f16_f32 v52, v34, v35
	v_pk_add_f32 v[34:35], v[144:145], v[36:37]
	ds_write2_b64 v155, v[82:83], v[86:87] offset0:12 offset1:14
	v_pk_mul_f32 v[82:83], v[202:203], v[34:35] op_sel_hi:[0,1]
	global_load_dwordx4 v[34:37], v154, s[0:1] offset:480
	s_waitcnt vmcnt(6)
	v_pk_add_f32 v[38:39], v[130:131], v[38:39]
	v_pk_add_f32 v[40:41], v[132:133], v[40:41]
	v_pk_mul_f32 v[38:39], v[202:203], v[38:39] op_sel_hi:[0,1]
	v_pk_mul_f32 v[40:41], v[202:203], v[40:41] op_sel_hi:[0,1]
	v_cvt_pk_f16_f32 v53, v82, v83
	v_cvt_pk_f16_f32 v38, v38, v39
	v_cvt_pk_f16_f32 v39, v40, v41
	ds_write2_b64 v176, v[52:53], v[38:39] offset0:80 offset1:82
	s_waitcnt vmcnt(5)
	v_pk_add_f32 v[38:39], v[138:139], v[58:59]
	v_pk_add_f32 v[40:41], v[140:141], v[60:61]
	v_pk_mul_f32 v[38:39], v[202:203], v[38:39] op_sel_hi:[0,1]
	v_pk_mul_f32 v[40:41], v[202:203], v[40:41] op_sel_hi:[0,1]
	v_cvt_pk_f16_f32 v38, v38, v39
	v_cvt_pk_f16_f32 v39, v40, v41
	v_pk_add_f32 v[40:41], v[138:139], v[42:43]
	v_pk_add_f32 v[42:43], v[140:141], v[44:45]
	v_pk_mul_f32 v[40:41], v[202:203], v[40:41] op_sel_hi:[0,1]
	v_pk_mul_f32 v[42:43], v[202:203], v[42:43] op_sel_hi:[0,1]
	v_cvt_pk_f16_f32 v40, v40, v41
	v_cvt_pk_f16_f32 v41, v42, v43
	v_pk_add_f32 v[54:55], v[130:131], v[54:55]
	v_pk_add_f32 v[56:57], v[132:133], v[56:57]
	v_pk_mul_f32 v[54:55], v[202:203], v[54:55] op_sel_hi:[0,1]
	v_pk_mul_f32 v[56:57], v[202:203], v[56:57] op_sel_hi:[0,1]
	v_cmp_gt_u32_e64 s[0:1], 8, v0
	v_cvt_pk_f16_f32 v54, v54, v55
	v_cvt_pk_f16_f32 v55, v56, v57
	s_and_b64 s[6:7], s[20:21], s[0:1]
	ds_write2_b64 v155, v[50:51], v[54:55] offset0:16 offset1:18
	s_waitcnt vmcnt(4)
	v_pk_add_f32 v[42:43], v[66:67], v[62:63]
	s_waitcnt vmcnt(3)
	v_pk_add_f32 v[18:19], v[70:71], v[18:19]
	v_pk_add_f32 v[20:21], v[72:73], v[20:21]
	v_pk_add_f32 v[2:3], v[70:71], v[2:3]
	v_pk_add_f32 v[4:5], v[72:73], v[4:5]
	v_pk_mul_f32 v[18:19], v[202:203], v[18:19] op_sel_hi:[0,1]
	v_pk_mul_f32 v[20:21], v[202:203], v[20:21] op_sel_hi:[0,1]
	v_pk_mul_f32 v[2:3], v[202:203], v[2:3] op_sel_hi:[0,1]
	v_pk_mul_f32 v[4:5], v[202:203], v[4:5] op_sel_hi:[0,1]
	v_cvt_pk_f16_f32 v18, v18, v19
	v_cvt_pk_f16_f32 v19, v20, v21
	v_cvt_pk_f16_f32 v2, v2, v3
	v_cvt_pk_f16_f32 v3, v4, v5
	s_waitcnt vmcnt(2)
	v_pk_add_f32 v[4:5], v[74:75], v[22:23]
	v_pk_add_f32 v[20:21], v[76:77], v[24:25]
	v_pk_mul_f32 v[4:5], v[202:203], v[4:5] op_sel_hi:[0,1]
	v_pk_mul_f32 v[20:21], v[202:203], v[20:21] op_sel_hi:[0,1]
	v_cvt_pk_f16_f32 v4, v4, v5
	v_cvt_pk_f16_f32 v5, v20, v21
	ds_write2_b64 v155, v[18:19], v[4:5] offset0:24 offset1:26
	v_pk_add_f32 v[4:5], v[74:75], v[6:7]
	v_pk_add_f32 v[6:7], v[76:77], v[8:9]
	v_pk_mul_f32 v[4:5], v[202:203], v[4:5] op_sel_hi:[0,1]
	v_pk_mul_f32 v[6:7], v[202:203], v[6:7] op_sel_hi:[0,1]
	v_cvt_pk_f16_f32 v4, v4, v5
	v_cvt_pk_f16_f32 v5, v6, v7
	ds_write2_b64 v176, v[2:3], v[4:5] offset0:88 offset1:90
	s_waitcnt vmcnt(1)
	v_pk_add_f32 v[2:3], v[78:79], v[26:27]
	v_pk_add_f32 v[4:5], v[80:81], v[28:29]
	v_pk_mul_f32 v[2:3], v[202:203], v[2:3] op_sel_hi:[0,1]
	v_pk_mul_f32 v[4:5], v[202:203], v[4:5] op_sel_hi:[0,1]
	v_cvt_pk_f16_f32 v2, v2, v3
	v_cvt_pk_f16_f32 v3, v4, v5
	v_pk_add_f32 v[4:5], v[78:79], v[10:11]
	v_pk_add_f32 v[6:7], v[80:81], v[12:13]
	v_pk_mul_f32 v[4:5], v[202:203], v[4:5] op_sel_hi:[0,1]
	v_pk_mul_f32 v[6:7], v[202:203], v[6:7] op_sel_hi:[0,1]
	v_pk_add_f32 v[44:45], v[68:69], v[64:65]
	v_cvt_pk_f16_f32 v4, v4, v5
	v_cvt_pk_f16_f32 v5, v6, v7
	s_waitcnt vmcnt(0)
	v_pk_add_f32 v[6:7], v[34:35], v[30:31]
	v_pk_add_f32 v[8:9], v[36:37], v[32:33]
	v_pk_mul_f32 v[42:43], v[202:203], v[42:43] op_sel_hi:[0,1]
	v_pk_mul_f32 v[44:45], v[202:203], v[44:45] op_sel_hi:[0,1]
	v_pk_mul_f32 v[6:7], v[202:203], v[6:7] op_sel_hi:[0,1]
	v_pk_mul_f32 v[8:9], v[202:203], v[8:9] op_sel_hi:[0,1]
	v_cvt_pk_f16_f32 v42, v42, v43
	v_cvt_pk_f16_f32 v43, v44, v45
	v_cvt_pk_f16_f32 v6, v6, v7
	v_cvt_pk_f16_f32 v7, v8, v9
	ds_write2_b64 v155, v[38:39], v[42:43] offset0:20 offset1:22
	v_pk_add_f32 v[38:39], v[66:67], v[46:47]
	v_pk_add_f32 v[42:43], v[68:69], v[48:49]
	ds_write2_b64 v155, v[2:3], v[6:7] offset0:28 offset1:30
	v_pk_add_f32 v[2:3], v[34:35], v[14:15]
	v_pk_add_f32 v[6:7], v[36:37], v[16:17]
	v_pk_mul_f32 v[38:39], v[202:203], v[38:39] op_sel_hi:[0,1]
	v_pk_mul_f32 v[42:43], v[202:203], v[42:43] op_sel_hi:[0,1]
	v_pk_mul_f32 v[2:3], v[202:203], v[2:3] op_sel_hi:[0,1]
	v_pk_mul_f32 v[6:7], v[202:203], v[6:7] op_sel_hi:[0,1]
	v_cvt_pk_f16_f32 v38, v38, v39
	v_cvt_pk_f16_f32 v39, v42, v43
	v_cvt_pk_f16_f32 v2, v2, v3
	v_cvt_pk_f16_f32 v3, v6, v7
	ds_write2_b64 v176, v[40:41], v[38:39] offset0:84 offset1:86
	ds_write2_b64 v176, v[4:5], v[2:3] offset0:92 offset1:94
	s_and_saveexec_b64 s[4:5], s[6:7]
	v_lshl_add_u32 v2, v0, 2, 0
	v_add_u32_e32 v2, 0x20800, v2
	v_mov_b32_e32 v3, 0
	ds_write_b32 v2, v3
	s_or_b64 exec, exec, s[4:5]
	s_waitcnt lgkmcnt(0)
	s_barrier
	s_mov_b64 s[4:5], -1
	s_and_b64 vcc, exec, s[22:23]
	s_cbranch_vccnz .LBB1_7
	s_andn2_b64 vcc, exec, s[4:5]
	s_cbranch_vccz .LBB1_14
